# nca kernels: cbias + K/V LDS base-address setup block hoisted from behind the last tile ds_write (critical path to barrier 1) into the load-wait ladder; post-barrier cbias leftovers removed
# speedup vs baseline: 1.0012x; 1.0012x over previous
.LBB1_14:
	s_or_b64 exec, exec, s[14:15]
	s_movk_i32 s62, 0x80
	v_lshrrev_b32_e32 v127, 8, v0
	v_or_b32_e32 v128, s20, v62
	v_mad_u32_u24 v129, v127, 7, 0
	v_add_u32_e32 v130, v128, v129
	v_sub_u32_e32 v129, v129, v1
	v_cmp_gt_u32_e64 s[58:59], 11, v129
	v_cmp_gt_u32_e64 s[60:61], s62, v130
	s_and_b64 s[44:45], s[58:59], s[60:61]
	v_mad_u32_u24 v129, v127, 7, 1
	v_add_u32_e32 v130, v128, v129
	v_sub_u32_e32 v129, v129, v1
	v_cmp_gt_u32_e64 s[58:59], 11, v129
	v_cmp_gt_u32_e64 s[60:61], s62, v130
	s_and_b64 s[46:47], s[58:59], s[60:61]
	v_mad_u32_u24 v129, v127, 7, 2
	v_add_u32_e32 v130, v128, v129
	v_sub_u32_e32 v129, v129, v1
	v_cmp_gt_u32_e64 s[58:59], 11, v129
	v_cmp_gt_u32_e64 s[60:61], s62, v130
	s_and_b64 s[48:49], s[58:59], s[60:61]
	v_mad_u32_u24 v129, v127, 7, 3
	v_add_u32_e32 v130, v128, v129
	v_sub_u32_e32 v129, v129, v1
	v_cmp_gt_u32_e64 s[58:59], 11, v129
	v_cmp_gt_u32_e64 s[60:61], s62, v130
	s_and_b64 s[50:51], s[58:59], s[60:61]
	v_mad_u32_u24 v129, v127, 7, 4
	v_add_u32_e32 v130, v128, v129
	v_sub_u32_e32 v129, v129, v1
	v_cmp_gt_u32_e64 s[58:59], 11, v129
	v_cmp_gt_u32_e64 s[60:61], s62, v130
	s_and_b64 s[52:53], s[58:59], s[60:61]
	v_mad_u32_u24 v129, v127, 7, 5
	v_add_u32_e32 v130, v128, v129
	v_sub_u32_e32 v129, v129, v1
	v_cmp_gt_u32_e64 s[58:59], 11, v129
	v_cmp_gt_u32_e64 s[60:61], s62, v130
	s_and_b64 s[54:55], s[58:59], s[60:61]
	v_mad_u32_u24 v129, v127, 7, 6
	v_add_u32_e32 v130, v128, v129
	v_sub_u32_e32 v129, v129, v1
	v_cmp_gt_u32_e64 s[58:59], 11, v129
	v_cmp_gt_u32_e64 s[60:61], s62, v130
	s_and_b64 s[56:57], s[58:59], s[60:61]
	v_mov_b32_e32 v52, 1
	v_lshlrev_b16_sdwa v52, v52, v65 dst_sel:DWORD dst_unused:UNUSED_PAD src0_sel:DWORD src1_sel:WORD_1
	v_mul_i32_i24_e32 v51, -9, v64
	v_add_u16_e32 v52, v52, v64
	v_mul_u32_u24_e32 v52, 0xa0, v52
	v_add_lshl_u32 v51, v51, v0, 4
	s_waitcnt vmcnt(9)
	v_cndmask_b32_e32 v29, 0, v29, vcc
	v_cndmask_b32_e32 v28, 0, v28, vcc
	v_cndmask_b32_e32 v27, 0, v27, vcc
	v_cndmask_b32_e32 v26, 0, v26, vcc
	v_add3_u32 v51, 0, v52, v51
	ds_write_b128 v51, v[26:29]
	v_bfe_u32 v131, v0, 4, 2
	v_lshlrev_b32_e32 v131, 2, v131
	v_or_b32_e32 v132, s21, v63
	v_mov_b32_e32 v111, 0xff800000
	s_movk_i32 s63, 0xa0
	v_or_b32_e32 v135, 0, v131
	v_add_u32_e32 v136, v132, v135
	v_sub_u32_e32 v135, v135, v61
	v_cmp_gt_u32_e64 s[58:59], 11, v135
	v_cmp_gt_u32_e64 s[60:61], s62, v136
	s_and_b64 s[58:59], s[58:59], s[60:61]
	v_cndmask_b32_e64 v112, v111, 0, s[58:59]
	v_or_b32_e32 v135, 1, v131
	v_add_u32_e32 v136, v132, v135
	v_sub_u32_e32 v135, v135, v61
	v_cmp_gt_u32_e64 s[58:59], 11, v135
	v_cmp_gt_u32_e64 s[60:61], s62, v136
	s_and_b64 s[58:59], s[58:59], s[60:61]
	v_cndmask_b32_e64 v113, v111, 0, s[58:59]
	v_or_b32_e32 v135, 2, v131
	v_add_u32_e32 v136, v132, v135
	v_sub_u32_e32 v135, v135, v61
	v_cmp_gt_u32_e64 s[58:59], 11, v135
	v_cmp_gt_u32_e64 s[60:61], s62, v136
	s_and_b64 s[58:59], s[58:59], s[60:61]
	v_cndmask_b32_e64 v114, v111, 0, s[58:59]
	v_or_b32_e32 v135, 3, v131
	v_add_u32_e32 v136, v132, v135
	v_sub_u32_e32 v135, v135, v61
	v_cmp_gt_u32_e64 s[58:59], 11, v135
	v_cmp_gt_u32_e64 s[60:61], s62, v136
	s_and_b64 s[58:59], s[58:59], s[60:61]
	v_cndmask_b32_e64 v115, v111, 0, s[58:59]
	v_lshrrev_b32_e32 v110, 8, v0
	v_mad_u32_u24 v136, v110, 7, v62
	v_mad_u32_u24 v98, v136, 20, v63
	v_and_b32_e32 v134, 15, v0
	v_add_u32_e32 v134, v98, v134
	v_mul_lo_u32 v134, v134, s63
	v_add_u32_e32 v99, 0, v134
	v_lshl_add_u32 v94, v131, 2, v99
	v_lshlrev_b16_e32 v27, 1, v67
	v_mul_i32_i24_e32 v26, -9, v66
	v_add_u16_e32 v27, v27, v66
	v_mul_u32_u24_e32 v27, 0xa0, v27
	v_add_lshl_u32 v26, v26, v59, 4
	s_waitcnt vmcnt(8)
	v_cndmask_b32_e64 v33, 0, v33, s[2:3]
	v_cndmask_b32_e64 v32, 0, v32, s[2:3]
	v_cndmask_b32_e64 v31, 0, v31, s[2:3]
	v_cndmask_b32_e64 v30, 0, v30, s[2:3]
	v_add3_u32 v26, 0, v27, v26
	v_lshlrev_b16_e32 v27, 1, v69
	ds_write_b128 v26, v[30:33]
	v_mul_i32_i24_e32 v26, -9, v68
	v_add_u16_e32 v27, v27, v68
	v_mul_u32_u24_e32 v27, 0xa0, v27
	v_add_lshl_u32 v26, v26, v58, 4
	s_waitcnt vmcnt(7)
	v_cndmask_b32_e64 v37, 0, v37, s[4:5]
	v_cndmask_b32_e64 v36, 0, v36, s[4:5]
	v_cndmask_b32_e64 v35, 0, v35, s[4:5]
	v_cndmask_b32_e64 v34, 0, v34, s[4:5]
	v_add3_u32 v26, 0, v27, v26
	v_lshlrev_b16_e32 v27, 1, v72
	ds_write_b128 v26, v[34:37]
	v_mul_i32_i24_e32 v26, -9, v71
	v_add_u16_e32 v27, v27, v71
	v_mul_u32_u24_e32 v27, 0xa0, v27
	v_add_lshl_u32 v26, v26, v70, 4
	v_mul_u32_u24_e32 v28, 0xca5, v73
	s_waitcnt vmcnt(6)
	v_cndmask_b32_e64 v45, 0, v45, s[8:9]
	v_cndmask_b32_e64 v44, 0, v44, s[8:9]
	v_cndmask_b32_e64 v43, 0, v43, s[8:9]
	v_cndmask_b32_e64 v42, 0, v42, s[8:9]
	v_add3_u32 v26, 0, v27, v26
	v_lshrrev_b32_e32 v28, 18, v28
	ds_write_b128 v26, v[42:45]
	v_mul_u32_u24_e32 v27, 0x1c72, v73
	v_mov_b32_e32 v26, -9
	v_and_b32_e32 v28, 62, v28
	v_mul_i32_i24_sdwa v29, v27, v26 dst_sel:DWORD dst_unused:UNUSED_PAD src0_sel:WORD_1 src1_sel:DWORD
	v_add_u16_sdwa v27, v28, v27 dst_sel:DWORD dst_unused:UNUSED_PAD src0_sel:DWORD src1_sel:WORD_1
	v_mul_u32_u24_e32 v27, 0xa0, v27
	v_add_lshl_u32 v28, v29, v73, 4
	s_movk_i32 s2, 0x164
	v_bfe_u32 v50, v0, 4, 2
	s_waitcnt vmcnt(5)
	v_cndmask_b32_e64 v49, 0, v49, s[10:11]
	v_cndmask_b32_e64 v48, 0, v48, s[10:11]
	v_cndmask_b32_e64 v47, 0, v47, s[10:11]
	v_cndmask_b32_e64 v46, 0, v46, s[10:11]
	v_add3_u32 v27, 0, v27, v28
	v_cmp_gt_u32_e32 vcc, s2, v0
	ds_write_b128 v27, v[46:49]
	s_and_saveexec_b64 s[2:3], vcc
	s_cbranch_execz .LBB1_16
	v_mul_u32_u24_e32 v32, 0xca5, v74
	v_lshrrev_b32_e32 v32, 18, v32
	v_mul_u32_u24_e32 v27, 0x1c72, v74
	v_and_b32_e32 v32, 62, v32
	v_mul_i32_i24_sdwa v26, v27, v26 dst_sel:DWORD dst_unused:UNUSED_PAD src0_sel:WORD_1 src1_sel:DWORD
	v_add_u16_sdwa v27, v32, v27 dst_sel:DWORD dst_unused:UNUSED_PAD src0_sel:DWORD src1_sel:WORD_1
	v_mul_u32_u24_e32 v27, 0xa0, v27
	v_add_lshl_u32 v26, v26, v74, 4
	s_waitcnt vmcnt(4)
	v_cndmask_b32_e64 v31, 0, v41, s[6:7]
	v_cndmask_b32_e64 v30, 0, v40, s[6:7]
	v_cndmask_b32_e64 v29, 0, v39, s[6:7]
	v_cndmask_b32_e64 v28, 0, v38, s[6:7]
	v_add3_u32 v26, 0, v27, v26
	ds_write_b128 v26, v[28:31]
.LBB1_16:
	s_or_b64 exec, exec, s[2:3]
	s_movk_i32 s2, 0x168
	s_waitcnt vmcnt(4)
	v_and_b32_e32 v39, 63, v0
	v_and_b32_e32 v40, 15, v0
	v_lshlrev_b32_e32 v26, 3, v50
	v_cmp_gt_u32_e32 vcc, s2, v0
	s_and_saveexec_b64 s[2:3], vcc
	s_movk_i32 s4, 0xa0
	v_mad_u32_u24 v27, v0, s4, 0
	v_mov_b32_e32 v28, 0x3c00
	ds_write_b16 v27, v28 offset:144
	s_or_b64 exec, exec, s[2:3]
	v_lshlrev_b32_e32 v38, 2, v50
	v_mad_u32_u24 v41, v110, 7, v62
	s_movk_i32 s6, 0xa0
	s_movk_i32 s7, 0x80
	s_waitcnt lgkmcnt(0)
	s_barrier
	ds_read_b128 v[26:29], v94
	ds_read_b128 v[34:37], v94 offset:64
	v_cndmask_b32_e64 v30, v111, v112, s[44:45]
	v_cndmask_b32_e64 v33, v111, v115, s[44:45]
	v_cndmask_b32_e64 v32, v111, v114, s[44:45]
	v_cndmask_b32_e64 v31, v111, v113, s[44:45]
	v_cmp_gt_u32_e32 vcc, 16, v39
	v_add_u32_e32 v98, v98, v38
	s_waitcnt lgkmcnt(1)
	v_mfma_f32_16x16x32_f16 v[30:33], v[26:29], v[10:13], v[30:33]
	ds_read_b128 v[42:45], v99 offset:128
	ds_read_b128 v[46:49], v94 offset:3200
	v_cndmask_b32_e32 v29, 0, v25, vcc
	s_waitcnt lgkmcnt(2)
	v_mfma_f32_16x16x32_f16 v[30:33], v[34:37], v[2:5], v[30:33]
	v_cndmask_b32_e32 v28, 0, v24, vcc
	v_cndmask_b32_e32 v27, 0, v23, vcc
	v_cndmask_b32_e32 v26, 0, v22, vcc
	ds_read_b128 v[34:37], v94 offset:3264
	ds_read_b128 v[50:53], v99 offset:3328
	s_waitcnt lgkmcnt(3)
	v_mfma_f32_16x16x32_f16 v[22:25], v[42:45], v[26:29], v[30:33]
	ds_read_b128 v[42:45], v94 offset:6400
	ds_read_b128 v[62:65], v94 offset:6464
	v_or_b32_e32 v98, v98, v1
	v_cndmask_b32_e64 v30, v111, v112, s[46:47]
	v_cndmask_b32_e64 v33, v111, v115, s[46:47]
	v_cndmask_b32_e64 v32, v111, v114, s[46:47]
	v_cndmask_b32_e64 v31, v111, v113, s[46:47]
	v_mul_lo_u32 v98, v98, s6
	v_lshlrev_b32_e32 v61, 3, v61
	s_waitcnt lgkmcnt(4)
	v_mfma_f32_16x16x32_f16 v[30:33], v[46:49], v[10:13], v[30:33]
	ds_read_b128 v[46:49], v99 offset:6528
	ds_read_b128 v[66:69], v94 offset:9600
	v_add3_u32 v61, 0, v98, v61
	s_waitcnt lgkmcnt(5)
	v_mfma_f32_16x16x32_f16 v[30:33], v[34:37], v[2:5], v[30:33]
	v_cndmask_b32_e64 v34, v111, v112, s[48:49]
	v_cndmask_b32_e64 v37, v111, v115, s[48:49]
	v_cndmask_b32_e64 v36, v111, v114, s[48:49]
	v_cndmask_b32_e64 v35, v111, v113, s[48:49]
	ds_read_b128 v[70:73], v94 offset:9664
	ds_read_b128 v[74:77], v99 offset:9728
	s_waitcnt lgkmcnt(6)
	v_mfma_f32_16x16x32_f16 v[30:33], v[50:53], v[26:29], v[30:33]
	ds_read_b128 v[50:53], v94 offset:12800
	ds_read_b128 v[78:81], v94 offset:12864
	s_waitcnt lgkmcnt(7)
	v_mfma_f32_16x16x32_f16 v[34:37], v[42:45], v[10:13], v[34:37]
	ds_read_b128 v[42:45], v99 offset:12928
	ds_read_b128 v[82:85], v94 offset:16000
	s_waitcnt lgkmcnt(8)
	v_mfma_f32_16x16x32_f16 v[34:37], v[62:65], v[2:5], v[34:37]
	ds_read_b128 v[62:65], v94 offset:16064
	ds_read_b128 v[86:89], v99 offset:16128
	v_mul_u32_u24_e32 v128, 0xa0, v60
	s_waitcnt lgkmcnt(9)
	v_mfma_f32_16x16x32_f16 v[34:37], v[46:49], v[26:29], v[34:37]
	v_cndmask_b32_e64 v46, v111, v112, s[50:51]
	v_cndmask_b32_e64 v49, v111, v115, s[50:51]
	v_cndmask_b32_e64 v48, v111, v114, s[50:51]
	v_cndmask_b32_e64 v47, v111, v113, s[50:51]
	ds_read_b128 v[90:93], v94 offset:19200
	ds_read_b128 v[94:97], v94 offset:19264
	s_waitcnt lgkmcnt(10)
	v_mfma_f32_16x16x32_f16 v[46:49], v[66:69], v[10:13], v[46:49]
	ds_read_b128 v[66:69], v99 offset:19328
	ds_read_b64_tr_b16 v[100:101], v61 offset:3200
	v_lshlrev_b32_e32 v129, 1, v56
	s_waitcnt lgkmcnt(11)
	v_mfma_f32_16x16x32_f16 v[46:49], v[70:73], v[2:5], v[46:49]
	ds_read_b64_tr_b16 v[98:99], v61
	ds_read_b64_tr_b16 v[70:71], v61 offset:32
	s_waitcnt lgkmcnt(12)
	v_mfma_f32_16x16x32_f16 v[46:49], v[74:77], v[26:29], v[46:49]
	v_cndmask_b32_e64 v74, v111, v112, s[52:53]
	v_cndmask_b32_e64 v77, v111, v115, s[52:53]
	v_cndmask_b32_e64 v76, v111, v114, s[52:53]
	v_cndmask_b32_e64 v75, v111, v113, s[52:53]
	ds_read_b64_tr_b16 v[72:73], v61 offset:3232
	ds_read_b64_tr_b16 v[102:103], v61 offset:64
	s_waitcnt lgkmcnt(13)
	v_mfma_f32_16x16x32_f16 v[50:53], v[50:53], v[10:13], v[74:77]
	ds_read_b64_tr_b16 v[104:105], v61 offset:3264
	v_add3_u32 v128, 0, v128, v129
	s_movk_i32 s4, 0xe39
	ds_read_b64_tr_b16 v[74:75], v61 offset:96
	s_waitcnt lgkmcnt(14)
	v_mfma_f32_16x16x32_f16 v[50:53], v[78:81], v[2:5], v[50:53]
	ds_read_b64_tr_b16 v[76:77], v61 offset:3296
	ds_read_b64_tr_b16 v[78:79], v61 offset:128
	s_movk_i32 s5, 0xffee
	s_waitcnt lgkmcnt(14)
	v_mfma_f32_16x16x32_f16 v[42:45], v[42:45], v[26:29], v[50:53]
	ds_read_b64_tr_b16 v[80:81], v61 offset:3328
	ds_read_b64_tr_b16 v[106:107], v61 offset:6400
	v_cndmask_b32_e64 v50, v111, v112, s[54:55]
	v_cndmask_b32_e64 v53, v111, v115, s[54:55]
	v_cndmask_b32_e64 v52, v111, v114, s[54:55]
	v_cndmask_b32_e64 v51, v111, v113, s[54:55]
	s_nop 0
	v_mfma_f32_16x16x32_f16 v[50:53], v[82:85], v[10:13], v[50:53]
	ds_read_b64_tr_b16 v[108:109], v61 offset:9600
	ds_read_b64_tr_b16 v[82:83], v61 offset:6432
	s_waitcnt lgkmcnt(14)
	v_mfma_f32_16x16x32_f16 v[50:53], v[62:65], v[2:5], v[50:53]
	ds_read_b64_tr_b16 v[84:85], v61 offset:9632
	ds_read_b64_tr_b16 v[62:63], v61 offset:6464
	v_mfma_f32_16x16x32_f16 v[50:53], v[86:89], v[26:29], v[50:53]
	v_cndmask_b32_e64 v86, v111, v112, s[56:57]
	v_cndmask_b32_e64 v89, v111, v115, s[56:57]
	v_cndmask_b32_e64 v88, v111, v114, s[56:57]
	v_cndmask_b32_e64 v87, v111, v113, s[56:57]
	ds_read_b64_tr_b16 v[64:65], v61 offset:9664
	ds_read_b64_tr_b16 v[110:111], v61 offset:6496
	v_mfma_f32_16x16x32_f16 v[10:13], v[90:93], v[10:13], v[86:89]
	s_mov_b32 s2, 0xff800000
	ds_read_b64_tr_b16 v[112:113], v61 offset:9696
	s_nop 0
	ds_read_b64_tr_b16 v[86:87], v61 offset:6528
	v_mfma_f32_16x16x32_f16 v[2:5], v[94:97], v[2:5], v[10:13]
	ds_read_b64_tr_b16 v[88:89], v61 offset:9728
	s_nop 1
	v_max3_f32 v12, v22, s2, v23
	v_max3_f32 v12, v12, v24, v25
	v_max3_f32 v12, v12, v30, v31
	v_max3_f32 v12, v12, v32, v33
	v_max3_f32 v12, v12, v34, v35
	v_max3_f32 v12, v12, v36, v37
	v_max3_f32 v12, v12, v46, v47
	v_max3_f32 v12, v12, v48, v49
	v_mbcnt_lo_u32_b32 v13, -1, 0
	ds_read_b64_tr_b16 v[10:11], v61 offset:12800
	s_waitcnt lgkmcnt(14)
	v_mfma_f32_16x16x32_f16 v[2:5], v[66:69], v[26:29], v[2:5]
	v_max3_f32 v12, v12, v42, v43
	v_mbcnt_hi_u32_b32 v13, -1, v13
	v_max3_f32 v12, v12, v44, v45
	v_and_b32_e32 v27, 64, v13
	v_max3_f32 v12, v12, v50, v51
	v_xor_b32_e32 v26, 16, v13
	v_add_u32_e32 v27, 64, v27
	v_max3_f32 v12, v12, v52, v53
	v_cmp_lt_i32_e32 vcc, v26, v27
	v_max3_f32 v12, v12, v2, v3
	v_max3_f32 v12, v12, v4, v5
	v_mov_b32_e32 v26, v12
	s_load_dwordx2 s[2:3], s[0:1], 0x20
	s_movk_i32 s0, 0x510
	v_permlane16_swap_b32_e32 v12, v26
	v_cmp_gt_u32_e32 vcc, 11, v41
	v_mov_b32_e32 v41, 0xc80
	v_max_f32_e32 v12, v12, v26
	v_mov_b32_e32 v13, v12
	s_nop 1
	v_permlane32_swap_b32_e32 v12, v13
	s_nop 1
	v_max_f32_e32 v26, v12, v13
	v_sub_f32_e32 v29, v34, v26
	v_exp_f32_e32 v92, v29
	v_sub_f32_e32 v29, v35, v26
	v_exp_f32_e32 v93, v29
	v_sub_f32_e32 v29, v36, v26
	v_exp_f32_e32 v36, v29
	v_sub_f32_e32 v29, v37, v26
	v_exp_f32_e32 v37, v29
	v_sub_f32_e32 v29, v46, v26
	v_exp_f32_e32 v94, v29
	v_sub_f32_e32 v29, v47, v26
	v_exp_f32_e32 v95, v29
	v_sub_f32_e32 v29, v48, v26
	v_sub_f32_e32 v13, v23, v26
	v_sub_f32_e32 v23, v25, v26
	v_sub_f32_e32 v25, v31, v26
	v_exp_f32_e32 v96, v29
	v_sub_f32_e32 v29, v49, v26
	v_sub_f32_e32 v12, v22, v26
	v_sub_f32_e32 v22, v24, v26
	v_sub_f32_e32 v24, v30, v26
	v_exp_f32_e32 v27, v25
	v_sub_f32_e32 v25, v32, v26
	v_sub_f32_e32 v28, v33, v26
	v_exp_f32_e32 v97, v29
	v_sub_f32_e32 v29, v42, v26
	v_exp_f32_e32 v12, v12
	v_exp_f32_e32 v13, v13
	v_exp_f32_e32 v22, v22
	v_exp_f32_e32 v23, v23
	v_exp_f32_e32 v24, v24
	v_exp_f32_e32 v25, v25
	v_exp_f32_e32 v28, v28
	v_exp_f32_e32 v114, v29
	v_sub_f32_e32 v29, v43, v26
	v_exp_f32_e32 v115, v29
	v_sub_f32_e32 v29, v44, v26
	v_exp_f32_e32 v116, v29
	v_sub_f32_e32 v29, v45, v26
	v_exp_f32_e32 v117, v29
	v_sub_f32_e32 v29, v50, v26
	v_exp_f32_e32 v118, v29
	v_sub_f32_e32 v29, v51, v26
	v_cvt_pk_f16_f32 v25, v25, v28
	v_cvt_pk_f16_f32 v24, v24, v27
	v_cvt_pk_f16_f32 v23, v22, v23
	v_cvt_pk_f16_f32 v22, v12, v13
	v_exp_f32_e32 v119, v29
	v_cndmask_b32_e32 v41, 0, v41, vcc
	s_waitcnt lgkmcnt(0)
	v_mfma_f32_16x16x32_f16 v[28:31], v[98:101], v[22:25], 0
	ds_read_b64_tr_b16 v[12:13], v61 offset:16000
	ds_read_b64_tr_b16 v[32:33], v61 offset:12832
	v_sub_f32_e32 v27, v52, v26
	v_mfma_f32_16x16x32_f16 v[42:45], v[70:73], v[22:25], 0
	ds_read_b64_tr_b16 v[34:35], v61 offset:16032
	ds_read_b64_tr_b16 v[46:47], v61 offset:12864
	v_exp_f32_e32 v27, v27
	v_mfma_f32_16x16x32_f16 v[66:69], v[102:105], v[22:25], 0
	ds_read_b64_tr_b16 v[48:49], v61 offset:16064
	ds_read_b64_tr_b16 v[70:71], v61 offset:12896
	v_sub_f32_e32 v2, v2, v26
	v_mfma_f32_16x16x32_f16 v[74:77], v[74:77], v[22:25], 0
	ds_read_b64_tr_b16 v[72:73], v61 offset:16096
	ds_read_b64_tr_b16 v[90:91], v61 offset:12928
	v_cmp_gt_u32_e32 vcc, s0, v58
	v_mfma_f32_16x16x32_f16 v[22:25], v[78:81], v[22:25], 0
	v_cvt_pk_f16_f32 v78, v92, v93
	ds_read_b64_tr_b16 v[92:93], v61 offset:16128
	v_cvt_pk_f16_f32 v81, v96, v97
	v_cvt_pk_f16_f32 v80, v94, v95
	v_cvt_pk_f16_f32 v79, v36, v37
	v_add_u32_e32 v36, v61, v41
	v_sub_f32_e32 v37, v53, v26
	ds_read_b64_tr_b16 v[94:95], v61 offset:19200
	v_mfma_f32_16x16x32_f16 v[28:31], v[106:109], v[78:81], v[28:31]
	ds_read_b64_tr_b16 v[96:97], v36 offset:19200
	ds_read_b64_tr_b16 v[100:101], v36 offset:19232
	v_exp_f32_e32 v37, v37
	v_mfma_f32_16x16x32_f16 v[42:45], v[82:85], v[78:81], v[42:45]
	ds_read_b64_tr_b16 v[98:99], v61 offset:19232
	ds_read_b64_tr_b16 v[50:51], v61 offset:19264
	v_mfma_f32_16x16x32_f16 v[62:65], v[62:65], v[78:81], v[66:69]
	ds_read_b64_tr_b16 v[52:53], v36 offset:19264
	s_nop 1
	ds_read_b64_tr_b16 v[66:67], v61 offset:19296
	v_mfma_f32_16x16x32_f16 v[74:77], v[110:113], v[78:81], v[74:77]
	ds_read_b64_tr_b16 v[68:69], v36 offset:19296
	ds_read_b64_tr_b16 v[82:83], v61 offset:19328
	v_mfma_f32_16x16x32_f16 v[22:25], v[86:89], v[78:81], v[22:25]
	ds_read_b64_tr_b16 v[84:85], v36 offset:19328
	s_waitcnt vmcnt(2)
	v_cvt_pk_f16_f32 v21, v20, v21
	v_cvt_pk_f16_f32 v20, v18, v19
	v_cvt_pk_f16_f32 v17, v16, v17
	v_cvt_pk_f16_f32 v16, v14, v15
	ds_write_b64 v128, v[20:21] offset:57600
	v_mul_u32_u24_sdwa v18, v59, s4 dst_sel:DWORD dst_unused:UNUSED_PAD src0_sel:WORD_0 src1_sel:DWORD
	v_mul_i32_i24_sdwa v19, v18, s5 dst_sel:DWORD dst_unused:UNUSED_PAD src0_sel:WORD_1 src1_sel:DWORD
	v_mul_u32_u24_sdwa v14, v18, s6 dst_sel:DWORD dst_unused:UNUSED_PAD src0_sel:WORD_1 src1_sel:DWORD
	v_add_lshl_u32 v15, v19, v59, 3
	v_exp_f32_e32 v18, v2
	v_sub_f32_e32 v19, v3, v26
	v_sub_f32_e32 v2, v4, v26
	v_sub_f32_e32 v21, v5, v26
	v_cvt_pk_f16_f32 v81, v27, v37
	v_cvt_pk_f16_f32 v80, v118, v119
	v_cvt_pk_f16_f32 v79, v116, v117
	v_cvt_pk_f16_f32 v78, v114, v115
	v_add3_u32 v14, 0, v14, v15
	v_exp_f32_e32 v20, v2
	v_exp_f32_e32 v21, v21
	v_exp_f32_e32 v19, v19
	s_waitcnt lgkmcnt(14)
	v_mfma_f32_16x16x32_f16 v[10:13], v[10:13], v[78:81], v[28:31]
	ds_write_b64 v14, v[16:17] offset:57600
	v_mfma_f32_16x16x32_f16 v[14:17], v[32:35], v[78:81], v[42:45]
	v_mfma_f32_16x16x32_f16 v[28:31], v[46:49], v[78:81], v[62:65]
	s_nop 1
	v_mov_b32_e32 v44, 0
	v_cvt_pk_f16_f32 v43, v20, v21
	v_cvt_pk_f16_f32 v42, v18, v19
	s_waitcnt lgkmcnt(14)
	v_mfma_f32_16x16x32_f16 v[2:5], v[70:73], v[78:81], v[74:77]
	v_mov_b32_e32 v45, v44
	s_waitcnt lgkmcnt(12)
	v_mfma_f32_16x16x32_f16 v[32:35], v[90:93], v[78:81], v[22:25]
	s_waitcnt lgkmcnt(10)
	v_mfma_f32_16x16x32_f16 v[22:25], v[94:97], v[42:45], v[10:13]
	s_waitcnt lgkmcnt(8)
	v_mfma_f32_16x16x32_f16 v[18:21], v[98:101], v[42:45], v[14:17]
	s_waitcnt lgkmcnt(6)
	v_mfma_f32_16x16x32_f16 v[14:17], v[50:53], v[42:45], v[28:31]
	s_waitcnt lgkmcnt(4)
	v_mfma_f32_16x16x32_f16 v[10:13], v[66:69], v[42:45], v[2:5]
	s_waitcnt lgkmcnt(2)
	v_mfma_f32_16x16x32_f16 v[2:5], v[82:85], v[42:45], v[32:35]
	s_and_saveexec_b64 s[0:1], vcc
	s_cbranch_execz .LBB1_20
	v_mul_u32_u24_sdwa v27, v58, s4 dst_sel:DWORD dst_unused:UNUSED_PAD src0_sel:WORD_0 src1_sel:DWORD
	v_mul_i32_i24_sdwa v28, v27, s5 dst_sel:DWORD dst_unused:UNUSED_PAD src0_sel:WORD_1 src1_sel:DWORD
	s_waitcnt vmcnt(1)
	v_cvt_pk_f16_f32 v9, v8, v9
	v_cvt_pk_f16_f32 v8, v6, v7
	v_mul_u32_u24_sdwa v6, v27, s6 dst_sel:DWORD dst_unused:UNUSED_PAD src0_sel:WORD_1 src1_sel:DWORD
	v_add_lshl_u32 v7, v28, v58, 3
	v_add3_u32 v6, 0, v6, v7
	ds_write_b64 v6, v[8:9] offset:57600

	.amdhsa_kernel _Z5k_ncaILi0EEvPKDF16_S1_PKfS3_PDF16_S3_S3_S3_S3_Pf
		.amdhsa_group_segment_fixed_size 0
		.amdhsa_private_segment_fixed_size 0
		.amdhsa_kernarg_size 80
		.amdhsa_user_sgpr_count 2
		.amdhsa_user_sgpr_dispatch_ptr 0
		.amdhsa_user_sgpr_queue_ptr 0
		.amdhsa_user_sgpr_kernarg_segment_ptr 1
		.amdhsa_user_sgpr_dispatch_id 0
		.amdhsa_user_sgpr_kernarg_preload_length 0
		.amdhsa_user_sgpr_kernarg_preload_offset 0
		.amdhsa_user_sgpr_private_segment_size 0
		.amdhsa_uses_dynamic_stack 0
		.amdhsa_enable_private_segment 0
		.amdhsa_system_sgpr_workgroup_id_x 1
		.amdhsa_system_sgpr_workgroup_id_y 0
		.amdhsa_system_sgpr_workgroup_id_z 0
		.amdhsa_system_sgpr_workgroup_info 0
		.amdhsa_system_vgpr_workitem_id 0
		.amdhsa_next_free_vgpr 169
		.amdhsa_next_free_sgpr 96
		.amdhsa_accum_offset 140
		.amdhsa_reserve_vcc 1
		.amdhsa_float_round_mode_32 0
		.amdhsa_float_round_mode_16_64 0
		.amdhsa_float_denorm_mode_32 3
		.amdhsa_float_denorm_mode_16_64 3
		.amdhsa_dx10_clamp 1
		.amdhsa_ieee_mode 1
		.amdhsa_fp16_overflow 0
		.amdhsa_tg_split 0
		.amdhsa_exception_fp_ieee_invalid_op 0
		.amdhsa_exception_fp_denorm_src 0
		.amdhsa_exception_fp_ieee_div_zero 0
		.amdhsa_exception_fp_ieee_overflow 0
		.amdhsa_exception_fp_ieee_underflow 0
		.amdhsa_exception_fp_ieee_inexact 0
		.amdhsa_exception_int_div_zero 0
	.end_amdhsa_kernel

.LBB2_14:
	s_or_b64 exec, exec, s[14:15]
	s_movk_i32 s62, 0x80
	v_lshrrev_b32_e32 v144, 8, v0
	v_or_b32_e32 v145, s29, v76
	v_mad_u32_u24 v146, v144, 7, 0
	v_add_u32_e32 v147, v145, v146
	v_sub_u32_e32 v146, v146, v60
	v_cmp_gt_u32_e64 s[58:59], 11, v146
	v_cmp_gt_u32_e64 s[60:61], s62, v147
	s_and_b64 s[44:45], s[58:59], s[60:61]
	v_mad_u32_u24 v146, v144, 7, 1
	v_add_u32_e32 v147, v145, v146
	v_sub_u32_e32 v146, v146, v60
	v_cmp_gt_u32_e64 s[58:59], 11, v146
	v_cmp_gt_u32_e64 s[60:61], s62, v147
	s_and_b64 s[46:47], s[58:59], s[60:61]
	v_mad_u32_u24 v146, v144, 7, 2
	v_add_u32_e32 v147, v145, v146
	v_sub_u32_e32 v146, v146, v60
	v_cmp_gt_u32_e64 s[58:59], 11, v146
	v_cmp_gt_u32_e64 s[60:61], s62, v147
	s_and_b64 s[48:49], s[58:59], s[60:61]
	v_mad_u32_u24 v146, v144, 7, 3
	v_add_u32_e32 v147, v145, v146
	v_sub_u32_e32 v146, v146, v60
	v_cmp_gt_u32_e64 s[58:59], 11, v146
	v_cmp_gt_u32_e64 s[60:61], s62, v147
	s_and_b64 s[50:51], s[58:59], s[60:61]
	v_mad_u32_u24 v146, v144, 7, 4
	v_add_u32_e32 v147, v145, v146
	v_sub_u32_e32 v146, v146, v60
	v_cmp_gt_u32_e64 s[58:59], 11, v146
	v_cmp_gt_u32_e64 s[60:61], s62, v147
	s_and_b64 s[52:53], s[58:59], s[60:61]
	v_mad_u32_u24 v146, v144, 7, 5
	v_add_u32_e32 v147, v145, v146
	v_sub_u32_e32 v146, v146, v60
	v_cmp_gt_u32_e64 s[58:59], 11, v146
	v_cmp_gt_u32_e64 s[60:61], s62, v147
	s_and_b64 s[54:55], s[58:59], s[60:61]
	v_mad_u32_u24 v146, v144, 7, 6
	v_add_u32_e32 v147, v145, v146
	v_sub_u32_e32 v146, v146, v60
	v_cmp_gt_u32_e64 s[58:59], 11, v146
	v_cmp_gt_u32_e64 s[60:61], s62, v147
	s_and_b64 s[56:57], s[58:59], s[60:61]
	v_mov_b32_e32 v52, 1
	v_lshlrev_b16_sdwa v52, v52, v78 dst_sel:DWORD dst_unused:UNUSED_PAD src0_sel:DWORD src1_sel:WORD_1
	v_mul_i32_i24_e32 v51, -9, v77
	v_add_u16_e32 v52, v52, v77
	v_mul_u32_u24_e32 v52, 0xa0, v52
	v_add_lshl_u32 v51, v51, v0, 4
	s_waitcnt vmcnt(17)
	v_cndmask_b32_e32 v29, 0, v29, vcc
	v_cndmask_b32_e32 v28, 0, v28, vcc
	v_cndmask_b32_e32 v27, 0, v27, vcc
	v_cndmask_b32_e32 v26, 0, v26, vcc
	v_add3_u32 v51, 0, v52, v51
	ds_write_b128 v51, v[26:29]
	v_bfe_u32 v144, v0, 4, 2
	v_lshlrev_b32_e32 v144, 2, v144
	v_or_b32_e32 v145, s30, v57
	v_mov_b32_e32 v51, 0xff800000
	s_movk_i32 s63, 0xa0
	v_or_b32_e32 v147, 0, v144
	v_add_u32_e32 v148, v145, v147
	v_sub_u32_e32 v147, v147, v1
	v_cmp_gt_u32_e64 s[58:59], 11, v147
	v_cmp_gt_u32_e64 s[60:61], s62, v148
	s_and_b64 s[58:59], s[58:59], s[60:61]
	v_cndmask_b32_e64 v52, v51, 0, s[58:59]
	v_or_b32_e32 v147, 1, v144
	v_add_u32_e32 v148, v145, v147
	v_sub_u32_e32 v147, v147, v1
	v_cmp_gt_u32_e64 s[58:59], 11, v147
	v_cmp_gt_u32_e64 s[60:61], s62, v148
	s_and_b64 s[58:59], s[58:59], s[60:61]
	v_cndmask_b32_e64 v53, v51, 0, s[58:59]
	v_or_b32_e32 v147, 2, v144
	v_add_u32_e32 v148, v145, v147
	v_sub_u32_e32 v147, v147, v1
	v_cmp_gt_u32_e64 s[58:59], 11, v147
	v_cmp_gt_u32_e64 s[60:61], s62, v148
	s_and_b64 s[58:59], s[58:59], s[60:61]
	v_cndmask_b32_e64 v128, v51, 0, s[58:59]
	v_or_b32_e32 v147, 3, v144
	v_add_u32_e32 v148, v145, v147
	v_sub_u32_e32 v147, v147, v1
	v_cmp_gt_u32_e64 s[58:59], 11, v147
	v_cmp_gt_u32_e64 s[60:61], s62, v148
	s_and_b64 s[58:59], s[58:59], s[60:61]
	v_cndmask_b32_e64 v129, v51, 0, s[58:59]
	v_lshrrev_b32_e32 v150, 8, v0
	v_mad_u32_u24 v148, v150, 7, v76
	v_mad_u32_u24 v116, v148, 20, v57
	v_and_b32_e32 v146, 15, v0
	v_add_u32_e32 v146, v116, v146
	v_mul_lo_u32 v146, v146, s63
	v_add_u32_e32 v117, 0, v146
	v_lshl_add_u32 v112, v144, 2, v117
	v_lshlrev_b16_e32 v27, 1, v80
	v_mul_i32_i24_e32 v26, -9, v79
	v_add_u16_e32 v27, v27, v79
	v_mul_u32_u24_e32 v27, 0xa0, v27
	v_add_lshl_u32 v26, v26, v62, 4
	s_waitcnt vmcnt(16)
	v_cndmask_b32_e64 v33, 0, v33, s[2:3]
	v_cndmask_b32_e64 v32, 0, v32, s[2:3]
	v_cndmask_b32_e64 v31, 0, v31, s[2:3]
	v_cndmask_b32_e64 v30, 0, v30, s[2:3]
	v_add3_u32 v26, 0, v27, v26
	v_lshlrev_b16_e32 v27, 1, v82
	ds_write_b128 v26, v[30:33]
	v_mul_i32_i24_e32 v26, -9, v81
	v_add_u16_e32 v27, v27, v81
	v_mul_u32_u24_e32 v27, 0xa0, v27
	v_add_lshl_u32 v26, v26, v61, 4
	s_waitcnt vmcnt(15)
	v_cndmask_b32_e64 v37, 0, v37, s[4:5]
	v_cndmask_b32_e64 v36, 0, v36, s[4:5]
	v_cndmask_b32_e64 v35, 0, v35, s[4:5]
	v_cndmask_b32_e64 v34, 0, v34, s[4:5]
	v_add3_u32 v26, 0, v27, v26
	v_lshlrev_b16_e32 v27, 1, v85
	ds_write_b128 v26, v[34:37]
	v_mul_i32_i24_e32 v26, -9, v84
	v_add_u16_e32 v27, v27, v84
	v_mul_u32_u24_e32 v27, 0xa0, v27
	v_add_lshl_u32 v26, v26, v83, 4
	v_mul_u32_u24_e32 v28, 0xca5, v86
	s_waitcnt vmcnt(14)
	v_cndmask_b32_e64 v45, 0, v45, s[8:9]
	v_cndmask_b32_e64 v44, 0, v44, s[8:9]
	v_cndmask_b32_e64 v43, 0, v43, s[8:9]
	v_cndmask_b32_e64 v42, 0, v42, s[8:9]
	v_add3_u32 v26, 0, v27, v26
	v_lshrrev_b32_e32 v28, 18, v28
	ds_write_b128 v26, v[42:45]
	v_mul_u32_u24_e32 v27, 0x1c72, v86
	v_mov_b32_e32 v26, -9
	v_and_b32_e32 v28, 62, v28
	v_mul_i32_i24_sdwa v29, v27, v26 dst_sel:DWORD dst_unused:UNUSED_PAD src0_sel:WORD_1 src1_sel:DWORD
	v_add_u16_sdwa v27, v28, v27 dst_sel:DWORD dst_unused:UNUSED_PAD src0_sel:DWORD src1_sel:WORD_1
	v_mul_u32_u24_e32 v27, 0xa0, v27
	v_add_lshl_u32 v28, v29, v86, 4
	s_movk_i32 s2, 0x164
	v_bfe_u32 v50, v0, 4, 2
	s_waitcnt vmcnt(13)
	v_cndmask_b32_e64 v49, 0, v49, s[10:11]
	v_cndmask_b32_e64 v48, 0, v48, s[10:11]
	v_cndmask_b32_e64 v47, 0, v47, s[10:11]
	v_cndmask_b32_e64 v46, 0, v46, s[10:11]
	v_add3_u32 v27, 0, v27, v28
	v_cmp_gt_u32_e32 vcc, s2, v0
	ds_write_b128 v27, v[46:49]
	s_and_saveexec_b64 s[2:3], vcc
	s_cbranch_execz .LBB2_16
	v_mul_u32_u24_e32 v32, 0xca5, v87
	v_lshrrev_b32_e32 v32, 18, v32
	v_mul_u32_u24_e32 v27, 0x1c72, v87
	v_and_b32_e32 v32, 62, v32
	v_mul_i32_i24_sdwa v26, v27, v26 dst_sel:DWORD dst_unused:UNUSED_PAD src0_sel:WORD_1 src1_sel:DWORD
	v_add_u16_sdwa v27, v32, v27 dst_sel:DWORD dst_unused:UNUSED_PAD src0_sel:DWORD src1_sel:WORD_1
	v_mul_u32_u24_e32 v27, 0xa0, v27
	v_add_lshl_u32 v26, v26, v87, 4
	s_waitcnt vmcnt(12)
	v_cndmask_b32_e64 v31, 0, v41, s[6:7]
	v_cndmask_b32_e64 v30, 0, v40, s[6:7]
	v_cndmask_b32_e64 v29, 0, v39, s[6:7]
	v_cndmask_b32_e64 v28, 0, v38, s[6:7]
	v_add3_u32 v26, 0, v27, v26
	ds_write_b128 v26, v[28:31]
.LBB2_16:
	s_or_b64 exec, exec, s[2:3]
	s_movk_i32 s2, 0x168
	s_waitcnt vmcnt(12)
	v_and_b32_e32 v38, 63, v0
	v_lshlrev_b32_e32 v26, 3, v50
	v_cmp_gt_u32_e32 vcc, s2, v0
	s_and_saveexec_b64 s[2:3], vcc
	s_movk_i32 s4, 0xa0
	v_mad_u32_u24 v27, v0, s4, 0
	v_mov_b32_e32 v28, 0x3c00
	ds_write_b16 v27, v28 offset:144
	s_or_b64 exec, exec, s[2:3]
	v_lshlrev_b32_e32 v39, 2, v50
	v_lshrrev_b32_e32 v41, 8, v0
	v_mad_u32_u24 v40, v41, 7, v76
	s_movk_i32 s6, 0xa0
	s_movk_i32 s7, 0x80
	s_waitcnt lgkmcnt(0)
	s_barrier
	ds_read_b128 v[26:29], v112
	ds_read_b128 v[34:37], v112 offset:64
	v_cndmask_b32_e64 v30, v51, v52, s[44:45]
	v_cndmask_b32_e64 v33, v51, v129, s[44:45]
	v_cndmask_b32_e64 v32, v51, v128, s[44:45]
	v_cndmask_b32_e64 v31, v51, v53, s[44:45]
	v_cmp_gt_u32_e32 vcc, 16, v38
	v_add_u32_e32 v116, v116, v39
	s_waitcnt lgkmcnt(1)
	v_mfma_f32_16x16x32_f16 v[30:33], v[26:29], v[10:13], v[30:33]
	ds_read_b128 v[42:45], v117 offset:128
	ds_read_b128 v[46:49], v112 offset:3200
	v_cndmask_b32_e32 v29, 0, v25, vcc
	s_waitcnt lgkmcnt(2)
	v_mfma_f32_16x16x32_f16 v[30:33], v[34:37], v[2:5], v[30:33]
	v_cndmask_b32_e32 v28, 0, v24, vcc
	v_cndmask_b32_e32 v27, 0, v23, vcc
	v_cndmask_b32_e32 v26, 0, v22, vcc
	ds_read_b128 v[34:37], v112 offset:3264
	ds_read_b128 v[76:79], v117 offset:3328
	s_waitcnt lgkmcnt(3)
	v_mfma_f32_16x16x32_f16 v[22:25], v[42:45], v[26:29], v[30:33]
	ds_read_b128 v[42:45], v112 offset:6400
	ds_read_b128 v[80:83], v112 offset:6464
	v_or_b32_e32 v116, v116, v60
	v_cndmask_b32_e64 v30, v51, v52, s[46:47]
	v_cndmask_b32_e64 v33, v51, v129, s[46:47]
	v_cndmask_b32_e64 v32, v51, v128, s[46:47]
	v_cndmask_b32_e64 v31, v51, v53, s[46:47]
	v_mul_lo_u32 v116, v116, s6
	s_waitcnt lgkmcnt(4)
	v_mfma_f32_16x16x32_f16 v[30:33], v[46:49], v[10:13], v[30:33]
	ds_read_b128 v[46:49], v117 offset:6528
	ds_read_b128 v[84:87], v112 offset:9600
	s_waitcnt lgkmcnt(5)
	v_mfma_f32_16x16x32_f16 v[30:33], v[34:37], v[2:5], v[30:33]
	v_cndmask_b32_e64 v34, v51, v52, s[48:49]
	v_cndmask_b32_e64 v37, v51, v129, s[48:49]
	v_cndmask_b32_e64 v36, v51, v128, s[48:49]
	v_cndmask_b32_e64 v35, v51, v53, s[48:49]
	ds_read_b128 v[88:91], v112 offset:9664
	ds_read_b128 v[92:95], v117 offset:9728
	s_waitcnt lgkmcnt(6)
	v_mfma_f32_16x16x32_f16 v[30:33], v[76:79], v[26:29], v[30:33]
	ds_read_b128 v[76:79], v112 offset:12800
	ds_read_b128 v[96:99], v112 offset:12864
	v_mul_u32_u24_e32 v146, 0xa0, v75
	s_waitcnt lgkmcnt(7)
	v_mfma_f32_16x16x32_f16 v[34:37], v[42:45], v[10:13], v[34:37]
	ds_read_b128 v[42:45], v117 offset:12928
	ds_read_b128 v[100:103], v112 offset:16000
	v_lshlrev_b32_e32 v147, 1, v54
	s_waitcnt lgkmcnt(8)
	v_mfma_f32_16x16x32_f16 v[34:37], v[80:83], v[2:5], v[34:37]
	ds_read_b128 v[80:83], v112 offset:16064
	ds_read_b128 v[104:107], v117 offset:16128
	v_add3_u32 v146, 0, v146, v147
	s_waitcnt lgkmcnt(9)
	v_mfma_f32_16x16x32_f16 v[34:37], v[46:49], v[26:29], v[34:37]
	v_cndmask_b32_e64 v46, v51, v52, s[50:51]
	v_cndmask_b32_e64 v49, v51, v129, s[50:51]
	v_cndmask_b32_e64 v48, v51, v128, s[50:51]
	v_cndmask_b32_e64 v47, v51, v53, s[50:51]
	ds_read_b128 v[108:111], v112 offset:19200
	ds_read_b128 v[112:115], v112 offset:19264
	s_waitcnt lgkmcnt(10)
	v_mfma_f32_16x16x32_f16 v[46:49], v[84:87], v[10:13], v[46:49]
	ds_read_b128 v[84:87], v117 offset:19328
	v_lshlrev_b32_e32 v117, 3, v1
	v_add3_u32 v132, 0, v116, v117
	ds_read_b64_tr_b16 v[118:119], v132 offset:3200
	s_waitcnt lgkmcnt(11)
	v_mfma_f32_16x16x32_f16 v[46:49], v[88:91], v[2:5], v[46:49]
	ds_read_b64_tr_b16 v[116:117], v132
	ds_read_b64_tr_b16 v[88:89], v132 offset:32
	s_waitcnt lgkmcnt(12)
	v_mfma_f32_16x16x32_f16 v[46:49], v[92:95], v[26:29], v[46:49]
	v_cndmask_b32_e64 v92, v51, v52, s[52:53]
	v_cndmask_b32_e64 v95, v51, v129, s[52:53]
	v_cndmask_b32_e64 v94, v51, v128, s[52:53]
	v_cndmask_b32_e64 v93, v51, v53, s[52:53]
	ds_read_b64_tr_b16 v[90:91], v132 offset:3232
	ds_read_b64_tr_b16 v[120:121], v132 offset:64
	s_waitcnt lgkmcnt(13)
	v_mfma_f32_16x16x32_f16 v[76:79], v[76:79], v[10:13], v[92:95]
	ds_read_b64_tr_b16 v[122:123], v132 offset:3264
	s_movk_i32 s8, 0xffee
	ds_read_b64_tr_b16 v[92:93], v132 offset:96
	s_waitcnt lgkmcnt(14)
	v_mfma_f32_16x16x32_f16 v[76:79], v[96:99], v[2:5], v[76:79]
	ds_read_b64_tr_b16 v[94:95], v132 offset:3296
	ds_read_b64_tr_b16 v[96:97], v132 offset:128
	s_waitcnt lgkmcnt(14)
	v_mfma_f32_16x16x32_f16 v[42:45], v[42:45], v[26:29], v[76:79]
	ds_read_b64_tr_b16 v[98:99], v132 offset:3328
	ds_read_b64_tr_b16 v[124:125], v132 offset:6400
	s_movk_i32 s4, 0x510
	v_cndmask_b32_e64 v76, v51, v52, s[54:55]
	v_cndmask_b32_e64 v79, v51, v129, s[54:55]
	v_cndmask_b32_e64 v78, v51, v128, s[54:55]
	v_cndmask_b32_e64 v77, v51, v53, s[54:55]
	s_nop 0
	v_mfma_f32_16x16x32_f16 v[76:79], v[100:103], v[10:13], v[76:79]
	ds_read_b64_tr_b16 v[126:127], v132 offset:9600
	ds_read_b64_tr_b16 v[100:101], v132 offset:6432
	s_waitcnt lgkmcnt(14)
	v_mfma_f32_16x16x32_f16 v[76:79], v[80:83], v[2:5], v[76:79]
	ds_read_b64_tr_b16 v[102:103], v132 offset:9632
	ds_read_b64_tr_b16 v[80:81], v132 offset:6464
	v_mfma_f32_16x16x32_f16 v[76:79], v[104:107], v[26:29], v[76:79]
	v_cndmask_b32_e64 v104, v51, v52, s[56:57]
	v_cndmask_b32_e64 v107, v51, v129, s[56:57]
	v_cndmask_b32_e64 v106, v51, v128, s[56:57]
	v_cndmask_b32_e64 v105, v51, v53, s[56:57]
	ds_read_b64_tr_b16 v[82:83], v132 offset:9664
	ds_read_b64_tr_b16 v[128:129], v132 offset:6496
	v_mfma_f32_16x16x32_f16 v[10:13], v[108:111], v[10:13], v[104:107]
	s_mov_b32 s2, 0xff800000
	ds_read_b64_tr_b16 v[130:131], v132 offset:9696
	s_movk_i32 s7, 0xe39
	ds_read_b64_tr_b16 v[104:105], v132 offset:6528
	v_mfma_f32_16x16x32_f16 v[2:5], v[112:115], v[2:5], v[10:13]
	ds_read_b64_tr_b16 v[106:107], v132 offset:9728
	s_nop 1
	v_max3_f32 v12, v22, s2, v23
	v_max3_f32 v12, v12, v24, v25
	v_max3_f32 v12, v12, v30, v31
	v_max3_f32 v12, v12, v32, v33
	v_max3_f32 v12, v12, v34, v35
	v_max3_f32 v12, v12, v36, v37
	v_max3_f32 v12, v12, v46, v47
	v_max3_f32 v12, v12, v48, v49
	v_mbcnt_lo_u32_b32 v13, -1, 0
	ds_read_b64_tr_b16 v[10:11], v132 offset:12800
	s_waitcnt lgkmcnt(14)
	v_mfma_f32_16x16x32_f16 v[2:5], v[84:87], v[26:29], v[2:5]
	v_max3_f32 v12, v12, v42, v43
	v_mbcnt_hi_u32_b32 v13, -1, v13
	v_max3_f32 v12, v12, v44, v45
	v_and_b32_e32 v27, 64, v13
	v_max3_f32 v12, v12, v76, v77
	v_xor_b32_e32 v26, 16, v13
	v_add_u32_e32 v27, 64, v27
	v_max3_f32 v12, v12, v78, v79
	v_cmp_lt_i32_e32 vcc, v26, v27
	v_max3_f32 v12, v12, v2, v3
	v_max3_f32 v12, v12, v4, v5
	v_mov_b32_e32 v26, v12
	v_cmp_lt_u32_e64 s[2:3], 15, v38
	s_nop 0
	v_permlane16_swap_b32_e32 v12, v26
	v_cmp_gt_u32_e32 vcc, 11, v40
	s_nop 0
	v_max_f32_e32 v12, v12, v26
	v_mov_b32_e32 v13, v12
	s_nop 1
	v_permlane32_swap_b32_e32 v12, v13
	s_nop 1
	v_max_f32_e32 v28, v12, v13
	v_sub_f32_e32 v12, v22, v28
	v_sub_f32_e32 v22, v24, v28
	v_sub_f32_e32 v24, v30, v28
	v_sub_f32_e32 v30, v35, v28
	v_exp_f32_e32 v41, v30
	v_sub_f32_e32 v30, v36, v28
	v_exp_f32_e32 v51, v30
	v_sub_f32_e32 v30, v37, v28
	v_exp_f32_e32 v52, v30
	v_sub_f32_e32 v30, v46, v28
	v_exp_f32_e32 v53, v30
	v_sub_f32_e32 v30, v47, v28
	v_exp_f32_e32 v110, v30
	v_sub_f32_e32 v30, v48, v28
	v_sub_f32_e32 v13, v23, v28
	v_sub_f32_e32 v23, v25, v28
	v_sub_f32_e32 v25, v31, v28
	v_exp_f32_e32 v111, v30
	v_sub_f32_e32 v30, v49, v28
	v_exp_f32_e32 v26, v25
	v_sub_f32_e32 v25, v32, v28
	v_sub_f32_e32 v27, v33, v28
	v_exp_f32_e32 v112, v30
	v_sub_f32_e32 v30, v42, v28
	v_exp_f32_e32 v12, v12
	v_exp_f32_e32 v13, v13
	v_exp_f32_e32 v22, v22
	v_exp_f32_e32 v23, v23
	v_exp_f32_e32 v24, v24
	v_exp_f32_e32 v25, v25
	v_exp_f32_e32 v27, v27
	v_exp_f32_e32 v133, v30
	v_sub_f32_e32 v30, v43, v28
	v_exp_f32_e32 v134, v30
	v_sub_f32_e32 v30, v44, v28
	v_exp_f32_e32 v135, v30
	v_sub_f32_e32 v30, v45, v28
	v_sub_f32_e32 v29, v34, v28
	v_exp_f32_e32 v136, v30
	v_sub_f32_e32 v30, v76, v28
	v_exp_f32_e32 v29, v29
	v_exp_f32_e32 v137, v30
	v_sub_f32_e32 v30, v77, v28
	v_cvt_pk_f16_f32 v25, v25, v27
	v_cvt_pk_f16_f32 v24, v24, v26
	v_cvt_pk_f16_f32 v23, v22, v23
	v_cvt_pk_f16_f32 v22, v12, v13
	v_exp_f32_e32 v138, v30
	v_mov_b32_e32 v27, 0xc80
	s_waitcnt lgkmcnt(0)
	v_mfma_f32_16x16x32_f16 v[30:33], v[116:119], v[22:25], 0
	ds_read_b64_tr_b16 v[12:13], v132 offset:16000
	ds_read_b64_tr_b16 v[34:35], v132 offset:12832
	v_cndmask_b32_e32 v27, 0, v27, vcc
	v_mfma_f32_16x16x32_f16 v[42:45], v[88:91], v[22:25], 0
	ds_read_b64_tr_b16 v[36:37], v132 offset:16032
	ds_read_b64_tr_b16 v[46:47], v132 offset:12864
	v_sub_f32_e32 v26, v78, v28
	v_mfma_f32_16x16x32_f16 v[84:87], v[120:123], v[22:25], 0
	ds_read_b64_tr_b16 v[48:49], v132 offset:16064
	ds_read_b64_tr_b16 v[88:89], v132 offset:12896
	v_add_u32_e32 v27, v132, v27
	v_mfma_f32_16x16x32_f16 v[92:95], v[92:95], v[22:25], 0
	ds_read_b64_tr_b16 v[90:91], v132 offset:16096
	ds_read_b64_tr_b16 v[108:109], v132 offset:12928
	v_exp_f32_e32 v26, v26
	v_mfma_f32_16x16x32_f16 v[22:25], v[96:99], v[22:25], 0
	v_cvt_pk_f16_f32 v99, v111, v112
	v_cvt_pk_f16_f32 v98, v53, v110
	ds_read_b64_tr_b16 v[110:111], v132 offset:16128
	v_cvt_pk_f16_f32 v97, v51, v52
	v_cvt_pk_f16_f32 v96, v29, v41
	v_sub_f32_e32 v29, v79, v28
	ds_read_b64_tr_b16 v[112:113], v132 offset:19200
	v_mfma_f32_16x16x32_f16 v[30:33], v[124:127], v[96:99], v[30:33]
	ds_read_b64_tr_b16 v[114:115], v27 offset:19200
	ds_read_b64_tr_b16 v[118:119], v27 offset:19232
	v_exp_f32_e32 v29, v29
	v_mfma_f32_16x16x32_f16 v[40:43], v[100:103], v[96:99], v[42:45]
	ds_read_b64_tr_b16 v[116:117], v132 offset:19232
	ds_read_b64_tr_b16 v[76:77], v132 offset:19264
	v_sub_f32_e32 v2, v2, v28
	v_mfma_f32_16x16x32_f16 v[80:83], v[80:83], v[96:99], v[84:87]
	ds_read_b64_tr_b16 v[78:79], v27 offset:19264
	v_cmp_gt_u32_e32 vcc, s4, v61
	s_nop 0
	ds_read_b64_tr_b16 v[84:85], v132 offset:19296
	v_mfma_f32_16x16x32_f16 v[92:95], v[128:131], v[96:99], v[92:95]
	ds_read_b64_tr_b16 v[86:87], v27 offset:19296
	ds_read_b64_tr_b16 v[100:101], v132 offset:19328
	v_mfma_f32_16x16x32_f16 v[22:25], v[104:107], v[96:99], v[22:25]
	ds_read_b64_tr_b16 v[102:103], v27 offset:19328
	s_waitcnt vmcnt(10)
	v_cvt_pk_f16_f32 v21, v20, v21
	v_cvt_pk_f16_f32 v20, v18, v19
	v_cvt_pk_f16_f32 v17, v16, v17
	v_cvt_pk_f16_f32 v16, v14, v15
	ds_write_b64 v146, v[20:21] offset:57600
	v_mul_u32_u24_sdwa v18, v62, s7 dst_sel:DWORD dst_unused:UNUSED_PAD src0_sel:WORD_0 src1_sel:DWORD
	v_mul_i32_i24_sdwa v19, v18, s8 dst_sel:DWORD dst_unused:UNUSED_PAD src0_sel:WORD_1 src1_sel:DWORD
	v_mul_u32_u24_sdwa v14, v18, s6 dst_sel:DWORD dst_unused:UNUSED_PAD src0_sel:WORD_1 src1_sel:DWORD
	v_add_lshl_u32 v15, v19, v62, 3
	v_exp_f32_e32 v18, v2
	v_sub_f32_e32 v19, v3, v28
	v_sub_f32_e32 v2, v4, v28
	v_sub_f32_e32 v21, v5, v28
	v_cvt_pk_f16_f32 v99, v26, v29
	v_cvt_pk_f16_f32 v98, v137, v138
	v_cvt_pk_f16_f32 v97, v135, v136
	v_cvt_pk_f16_f32 v96, v133, v134
	v_add3_u32 v14, 0, v14, v15
	v_exp_f32_e32 v20, v2
	v_exp_f32_e32 v21, v21
	v_exp_f32_e32 v19, v19
	s_waitcnt lgkmcnt(14)
	v_mfma_f32_16x16x32_f16 v[10:13], v[10:13], v[96:99], v[30:33]
	ds_write_b64 v14, v[16:17] offset:57600
	v_mfma_f32_16x16x32_f16 v[14:17], v[34:37], v[96:99], v[40:43]
	v_mfma_f32_16x16x32_f16 v[30:33], v[46:49], v[96:99], v[80:83]
	s_nop 1
	v_mov_b32_e32 v42, 0
	v_cvt_pk_f16_f32 v41, v20, v21
	v_cvt_pk_f16_f32 v40, v18, v19
	s_waitcnt lgkmcnt(14)
	v_mfma_f32_16x16x32_f16 v[2:5], v[88:91], v[96:99], v[92:95]
	v_mov_b32_e32 v43, v42
	s_waitcnt lgkmcnt(12)
	v_mfma_f32_16x16x32_f16 v[34:37], v[108:111], v[96:99], v[22:25]
	s_waitcnt lgkmcnt(10)
	v_mfma_f32_16x16x32_f16 v[22:25], v[112:115], v[40:43], v[10:13]
	s_waitcnt lgkmcnt(8)
	v_mfma_f32_16x16x32_f16 v[18:21], v[116:119], v[40:43], v[14:17]
	s_waitcnt lgkmcnt(6)
	v_mfma_f32_16x16x32_f16 v[14:17], v[76:79], v[40:43], v[30:33]
	s_waitcnt lgkmcnt(4)
	v_mfma_f32_16x16x32_f16 v[10:13], v[84:87], v[40:43], v[2:5]
	s_waitcnt lgkmcnt(2)
	v_mfma_f32_16x16x32_f16 v[2:5], v[100:103], v[40:43], v[34:37]
	s_and_saveexec_b64 s[4:5], vcc
	s_cbranch_execz .LBB2_20
	v_mul_u32_u24_sdwa v26, v61, s7 dst_sel:DWORD dst_unused:UNUSED_PAD src0_sel:WORD_0 src1_sel:DWORD
	v_mul_i32_i24_sdwa v27, v26, s8 dst_sel:DWORD dst_unused:UNUSED_PAD src0_sel:WORD_1 src1_sel:DWORD
	s_waitcnt vmcnt(8)
	v_cvt_pk_f16_f32 v9, v8, v9
	v_cvt_pk_f16_f32 v8, v6, v7
	v_mul_u32_u24_sdwa v6, v26, s6 dst_sel:DWORD dst_unused:UNUSED_PAD src0_sel:WORD_1 src1_sel:DWORD
	v_add_lshl_u32 v7, v27, v61, 3
	v_add3_u32 v6, 0, v6, v7
	ds_write_b64 v6, v[8:9] offset:57600

	.amdhsa_kernel _Z5k_ncaILi1EEvPKDF16_S1_PKfS3_PDF16_S3_S3_S3_S3_Pf
		.amdhsa_group_segment_fixed_size 0
		.amdhsa_private_segment_fixed_size 0
		.amdhsa_kernarg_size 80
		.amdhsa_user_sgpr_count 2
		.amdhsa_user_sgpr_dispatch_ptr 0
		.amdhsa_user_sgpr_queue_ptr 0
		.amdhsa_user_sgpr_kernarg_segment_ptr 1
		.amdhsa_user_sgpr_dispatch_id 0
		.amdhsa_user_sgpr_kernarg_preload_length 0
		.amdhsa_user_sgpr_kernarg_preload_offset 0
		.amdhsa_user_sgpr_private_segment_size 0
		.amdhsa_uses_dynamic_stack 0
		.amdhsa_enable_private_segment 0
		.amdhsa_system_sgpr_workgroup_id_x 1
		.amdhsa_system_sgpr_workgroup_id_y 0
		.amdhsa_system_sgpr_workgroup_id_z 0
		.amdhsa_system_sgpr_workgroup_info 0
		.amdhsa_system_vgpr_workitem_id 0
		.amdhsa_next_free_vgpr 169
		.amdhsa_next_free_sgpr 96
		.amdhsa_accum_offset 152
		.amdhsa_reserve_vcc 1
		.amdhsa_float_round_mode_32 0
		.amdhsa_float_round_mode_16_64 0
		.amdhsa_float_denorm_mode_32 3
		.amdhsa_float_denorm_mode_16_64 3
		.amdhsa_dx10_clamp 1
		.amdhsa_ieee_mode 1
		.amdhsa_fp16_overflow 0
		.amdhsa_tg_split 0
		.amdhsa_exception_fp_ieee_invalid_op 0
		.amdhsa_exception_fp_denorm_src 0
		.amdhsa_exception_fp_ieee_div_zero 0
		.amdhsa_exception_fp_ieee_overflow 0
		.amdhsa_exception_fp_ieee_underflow 0
		.amdhsa_exception_fp_ieee_inexact 0
		.amdhsa_exception_int_div_zero 0
	.end_amdhsa_kernel
